# v15: scan state waves at s_setprio 1 during the solve and chunks 0-1 of a round, 0 during chunks 2-3
# speedup vs baseline: 1.0168x; 1.0024x over previous
.LBB0_1734:
	s_cmp_lt_u32 s69, 2
	s_cbranch_scc0 .Lx_pr0
	s_setprio 1
	s_branch .Lx_prj
.Lx_pr0:
	s_setprio 0
.Lx_prj:
	s_mul_i32 s0, s69, 0x3300
	s_add_i32 s0, s74, s0
	s_add_i32 s1, s0, 0x2a00
	v_add_u32_e32 v18, s1, v185
	ds_read_b64_tr_b16 v[20:21], v18
	v_add3_u32 v18, s0, v186, v187
	ds_read2_b64 v[26:29], v18 offset1:4
	ds_read2_b64 v[30:33], v18 offset0:8 offset1:12
	v_add_u32_e32 v18, 0x800, v18
	v_cvt_pk_bf16_f32 v22, v2, v3
	v_cvt_pk_bf16_f32 v23, v4, v5
	v_cvt_pk_bf16_f32 v24, v10, v11
	v_cvt_pk_bf16_f32 v25, v12, v13
	ds_read2_b64 v[38:41], v18 offset0:32 offset1:36
	ds_read2_b64 v[42:45], v18 offset0:40 offset1:44
	s_waitcnt lgkmcnt(3)
	v_mfma_f32_16x16x32_bf16 v[26:29], v[26:29], v[22:25], 0
	s_waitcnt lgkmcnt(0)
	s_add_i32 s76, s69, s68
	v_cvt_pk_bf16_f32 v34, v6, v7
	v_cvt_pk_bf16_f32 v35, v8, v9
	v_cvt_pk_bf16_f32 v36, v14, v15
	v_cvt_pk_bf16_f32 v37, v16, v17
	s_waitcnt lgkmcnt(2)
	s_nop 0
	v_mfma_f32_16x16x32_bf16 v[26:29], v[30:33], v[34:37], v[26:29]
	s_nop 7
	v_cvt_pk_bf16_f32 v18, v26, v27
	v_add_u32_e32 v26, s0, v192
	ds_read_b128 v[30:33], v26 offset:8704
	v_add_u32_e32 v62, s0, v191
	ds_read_b128 v[46:49], v62 offset:12800
	v_cvt_pk_bf16_f32 v19, v28, v29
	ds_read_b128 v[26:29], v26 offset:9728
	ds_read_b128 v[50:53], v62 offset:12864
	v_add_u32_e32 v63, v62, v190
	ds_read_b128 v[54:57], v63 offset:4608
	ds_read_b128 v[58:61], v63 offset:5632
	s_waitcnt lgkmcnt(5)
	v_mfma_f32_16x16x32_bf16 v[30:33], v[30:33], v[18:21], 0
	s_waitcnt lgkmcnt(2)
	v_pk_mul_f32 v[10:11], v[10:11], v[50:51]
	v_pk_mul_f32 v[12:13], v[12:13], v[52:53]
	ds_read_b128 v[50:53], v63 offset:7680
	v_mfma_f32_16x16x32_bf16 v[22:25], v[38:41], v[22:25], 0
	s_nop 2
	v_cvt_pk_bf16_f32 v18, v30, v31
	v_cvt_pk_bf16_f32 v19, v32, v33
	ds_read_b128 v[30:33], v63 offset:6656
	v_pk_mul_f32 v[2:3], v[2:3], v[46:47]
	v_pk_mul_f32 v[4:5], v[4:5], v[48:49]
	ds_read_b128 v[46:49], v62 offset:12928
	v_mfma_f32_16x16x32_bf16 v[22:25], v[42:45], v[34:37], v[22:25]
	s_cmp_lt_u32 s76, 16
	s_waitcnt lgkmcnt(4)
	v_mfma_f32_16x16x32_bf16 v[2:5], v[54:57], v[18:21], v[2:5]
	ds_read_b128 v[54:57], v62 offset:12992
	s_waitcnt lgkmcnt(1)
	v_pk_mul_f32 v[6:7], v[6:7], v[46:47]
	v_pk_mul_f32 v[8:9], v[8:9], v[48:49]
	v_mfma_f32_16x16x32_bf16 v[10:13], v[58:61], v[18:21], v[10:13]
	s_waitcnt lgkmcnt(0)
	v_pk_mul_f32 v[14:15], v[14:15], v[54:55]
	v_pk_mul_f32 v[16:17], v[16:17], v[56:57]
	v_mfma_f32_16x16x32_bf16 v[6:9], v[30:33], v[18:21], v[6:9]
	s_nop 0
	v_mfma_f32_16x16x32_bf16 v[14:17], v[50:53], v[18:21], v[14:17]
	v_mfma_f32_16x16x32_bf16 v[18:21], v[26:29], v[18:21], v[22:25]
	s_cbranch_scc1 .LBB0_1731
	s_nop 6
	v_mov_b32_dpp v32, v18 quad_perm:[1,0,3,2] row_mask:0xf bank_mask:0xf bound_ctrl:1
	v_mov_b32_dpp v33, v19 quad_perm:[1,0,3,2] row_mask:0xf bank_mask:0xf bound_ctrl:1
	v_mov_b32_dpp v34, v20 quad_perm:[1,0,3,2] row_mask:0xf bank_mask:0xf bound_ctrl:1
	v_mov_b32_dpp v35, v21 quad_perm:[1,0,3,2] row_mask:0xf bank_mask:0xf bound_ctrl:1
	v_cndmask_b32_e64 v36, v18, v33, s[98:99]
	v_cndmask_b32_e64 v37, v32, v19, s[98:99]
	v_cndmask_b32_e64 v38, v20, v35, s[98:99]
	v_cndmask_b32_e64 v39, v34, v21, s[98:99]
	v_cvt_pk_bf16_f32 v36, v36, v37
	v_cvt_pk_bf16_f32 v38, v38, v39
	global_store_dword v[210:211], v36, off sc1
	global_store_dword v[212:213], v38, off sc1
	s_branch .LBB0_1731
